# v83 + read-once residual loads of the two out-projection epilogues marked non-temporal
# baseline (speedup 1.0000x reference)
; __device__ __forceinline__ u32x4 pack8(const f32x4 v0, const f32x4 v1) { u32x4 w; w.x = cvt_pk_bf16(v0[0], v0[1]); w.y = cvt_pk_bf16(v0[2], v0[3]); w.z = cvt_pk_bf16(v1[0], v1[1]); w.w = cvt_pk_bf16(v1[2], v1[3]); return w; }
; #define EPI_ROWLOOP for (int ai = 0; ai < 2; ++ai) _Pragma("unroll") for (int m = 0; m < 4; ++m)
;     __device__ __forceinline__ void operator()(const f32x4 (&acc)[2][2][4][2], const pg8::Unit& u, int wr, int wc, int fr, int fq) const {
;         const int row0 = u.pm * 256 + wr * 64 + fr, c0 = u.pn * 256 + wc * 32 + 8 * fq;
; #pragma unroll
;         EPI_ROWLOOP { const size_t ro = (size_t)(row0 + ai * 128 + m * 16) * 1024 + c0;
; #pragma unroll
;             for (int bj = 0; bj < 2; ++bj) {
;                 f32x4 r0, r1;
;                 if (resf) { r0 = *(const f32x4*)(resf + ro + bj * 128); r1 = *(const f32x4*)(resf + ro + bj * 128 + 4); }
;                 else { const u32x4 xv = *(const u32x4*)(resb + ro + bj * 128);
;                     r0[0] = __uint_as_float(xv.x << 16); r0[1] = __uint_as_float(xv.x & 0xffff0000u); r0[2] = __uint_as_float(xv.y << 16); r0[3] = __uint_as_float(xv.y & 0xffff0000u);
;                     r1[0] = __uint_as_float(xv.z << 16); r1[1] = __uint_as_float(xv.z & 0xffff0000u); r1[2] = __uint_as_float(xv.w << 16); r1[3] = __uint_as_float(xv.w & 0xffff0000u); }
;                 *(u32x4*)(Y + ro + bj * 128) = pack8(acc[ai][bj][m][0] * sc + r0 * ALPHA, acc[ai][bj][m][1] * sc + r1 * ALPHA);
;             } }
.LBB0_412:
	v_lshl_add_u32 v154, s58, 8, v139
	v_lshl_or_b32 v156, s61, 8, v140
	v_ashrrev_i32_e32 v155, 31, v154
	v_ashrrev_i32_e32 v157, 31, v156
	v_lshlrev_b64 v[134:135], 10, v[154:155]
	v_lshl_add_u64 v[134:135], v[134:135], 0, v[156:157]
	v_lshl_add_u64 v[158:159], v[134:135], 2, s[2:3]
	v_lshl_add_u64 v[160:161], v[134:135], 1, s[8:9]
	s_andn2_b64 vcc, exec, s[4:5]
	s_mov_b64 s[4:5], -1
	global_load_dwordx4 v[146:149], v[158:159], off nt
	s_nop 0
	global_load_dwordx4 v[150:153], v[158:159], off offset:16 nt
	global_load_dwordx4 v[162:165], v[158:159], off offset:512 nt
	s_nop 0
	global_load_dwordx4 v[166:169], v[158:159], off offset:528 nt
	s_mov_b64 s[98:99], 0x10000
	v_lshl_add_u64 v[250:251], v[158:159], 0, s[98:99]
	global_load_dwordx4 v[170:173], v[250:251], off nt
	s_nop 0
	global_load_dwordx4 v[174:177], v[250:251], off offset:16 nt
	global_load_dwordx4 v[178:181], v[250:251], off offset:512 nt
	s_nop 0
	global_load_dwordx4 v[182:185], v[250:251], off offset:528 nt
	s_mov_b64 s[98:99], 0x20000
	v_lshl_add_u64 v[250:251], v[158:159], 0, s[98:99]
	global_load_dwordx4 v[186:189], v[250:251], off nt
	s_nop 0
	global_load_dwordx4 v[190:193], v[250:251], off offset:16 nt
	global_load_dwordx4 v[194:197], v[250:251], off offset:512 nt
	s_nop 0
	global_load_dwordx4 v[198:201], v[250:251], off offset:528 nt
	s_mov_b64 s[98:99], 0x30000
	v_lshl_add_u64 v[250:251], v[158:159], 0, s[98:99]
	global_load_dwordx4 v[202:205], v[250:251], off nt
	s_nop 0
	global_load_dwordx4 v[206:209], v[250:251], off offset:16 nt
	global_load_dwordx4 v[226:229], v[250:251], off offset:512 nt
	s_nop 0
	global_load_dwordx4 v[230:233], v[250:251], off offset:528 nt
	s_mov_b64 s[98:99], 0x80000
	v_lshl_add_u64 v[250:251], v[158:159], 0, s[98:99]
	global_load_dwordx4 v[234:237], v[250:251], off nt
	s_nop 0
	global_load_dwordx4 v[238:241], v[250:251], off offset:16 nt
	global_load_dwordx4 v[242:245], v[250:251], off offset:512 nt
	s_nop 0
	global_load_dwordx4 v[246:249], v[250:251], off offset:528 nt
	s_mov_b64 s[98:99], 0x90000
	v_lshl_add_u64 v[250:251], v[158:159], 0, s[98:99]
	global_load_dwordx4 v[210:213], v[250:251], off nt
	s_nop 0
	global_load_dwordx4 v[214:217], v[250:251], off offset:16 nt
	global_load_dwordx4 v[218:221], v[250:251], off offset:512 nt
	s_nop 0
	global_load_dwordx4 v[222:225], v[250:251], off offset:528 nt
	s_waitcnt vmcnt(22)
	v_pk_fma_f32 v[128:129], v[148:149], s[12:13], v[128:129] op_sel_hi:[1,0,1]
	v_pk_fma_f32 v[126:127], v[146:147], s[12:13], v[126:127] op_sel_hi:[1,0,1]
	v_pk_fma_f32 v[146:147], v[152:153], s[12:13], v[124:125] op_sel_hi:[1,0,1]
	v_pk_fma_f32 v[124:125], v[150:151], s[12:13], v[122:123] op_sel_hi:[1,0,1]
	v_cvt_pk_bf16_f32 v122, v126, v127
	v_cvt_pk_bf16_f32 v123, v128, v129
	v_cvt_pk_bf16_f32 v124, v124, v125
	v_cvt_pk_bf16_f32 v125, v146, v147
	global_store_dwordx4 v[160:161], v[122:125], off
	s_mov_b64 s[98:99], 0xa0000
	v_lshl_add_u64 v[250:251], v[158:159], 0, s[98:99]
	global_load_dwordx4 v[122:125], v[250:251], off nt
	s_nop 0
	global_load_dwordx4 v[126:129], v[250:251], off offset:16 nt
	s_waitcnt vmcnt(23)
	v_pk_fma_f32 v[120:121], v[164:165], s[12:13], v[120:121] op_sel_hi:[1,0,1]
	v_pk_fma_f32 v[118:119], v[162:163], s[12:13], v[118:119] op_sel_hi:[1,0,1]
	v_pk_fma_f32 v[162:163], v[168:169], s[12:13], v[116:117] op_sel_hi:[1,0,1]
	v_pk_fma_f32 v[116:117], v[166:167], s[12:13], v[114:115] op_sel_hi:[1,0,1]
	v_cvt_pk_bf16_f32 v114, v118, v119
	v_cvt_pk_bf16_f32 v115, v120, v121
	v_cvt_pk_bf16_f32 v116, v116, v117
	v_cvt_pk_bf16_f32 v117, v162, v163
	global_store_dwordx4 v[160:161], v[114:117], off offset:256
	global_load_dwordx4 v[114:117], v[250:251], off offset:512 nt
	s_nop 0
	global_load_dwordx4 v[118:121], v[250:251], off offset:528 nt
	s_waitcnt vmcnt(24)
	v_pk_fma_f32 v[112:113], v[172:173], s[12:13], v[112:113] op_sel_hi:[1,0,1]
	v_pk_fma_f32 v[110:111], v[170:171], s[12:13], v[110:111] op_sel_hi:[1,0,1]
	v_pk_fma_f32 v[170:171], v[176:177], s[12:13], v[108:109] op_sel_hi:[1,0,1]
	v_pk_fma_f32 v[108:109], v[174:175], s[12:13], v[106:107] op_sel_hi:[1,0,1]
	v_cvt_pk_bf16_f32 v106, v110, v111
	v_cvt_pk_bf16_f32 v107, v112, v113
	v_cvt_pk_bf16_f32 v108, v108, v109
	v_cvt_pk_bf16_f32 v109, v170, v171
	s_mov_b64 s[98:99], 0x8000
	v_lshl_add_u64 v[254:255], v[160:161], 0, s[98:99]
	global_store_dwordx4 v[254:255], v[106:109], off
	s_mov_b64 s[98:99], 0xb0000
	v_lshl_add_u64 v[250:251], v[158:159], 0, s[98:99]
	global_load_dwordx4 v[106:109], v[250:251], off nt
	s_nop 0
	global_load_dwordx4 v[110:113], v[250:251], off offset:16 nt
	s_waitcnt vmcnt(25)
	v_pk_fma_f32 v[104:105], v[180:181], s[12:13], v[104:105] op_sel_hi:[1,0,1]
	v_pk_fma_f32 v[102:103], v[178:179], s[12:13], v[102:103] op_sel_hi:[1,0,1]
	v_pk_fma_f32 v[178:179], v[184:185], s[12:13], v[100:101] op_sel_hi:[1,0,1]
	v_pk_fma_f32 v[100:101], v[182:183], s[12:13], v[98:99] op_sel_hi:[1,0,1]
	v_cvt_pk_bf16_f32 v98, v102, v103
	v_cvt_pk_bf16_f32 v99, v104, v105
	v_cvt_pk_bf16_f32 v100, v100, v101
	v_cvt_pk_bf16_f32 v101, v178, v179
	global_store_dwordx4 v[254:255], v[98:101], off offset:256
	global_load_dwordx4 v[98:101], v[250:251], off offset:512 nt
	s_nop 0
	global_load_dwordx4 v[102:105], v[250:251], off offset:528 nt
	s_waitcnt vmcnt(26)
	v_pk_fma_f32 v[96:97], v[188:189], s[12:13], v[96:97] op_sel_hi:[1,0,1]
	v_pk_fma_f32 v[94:95], v[186:187], s[12:13], v[94:95] op_sel_hi:[1,0,1]
	v_pk_fma_f32 v[186:187], v[192:193], s[12:13], v[92:93] op_sel_hi:[1,0,1]
	v_pk_fma_f32 v[92:93], v[190:191], s[12:13], v[90:91] op_sel_hi:[1,0,1]
	v_cvt_pk_bf16_f32 v90, v94, v95
	v_cvt_pk_bf16_f32 v91, v96, v97
	v_cvt_pk_bf16_f32 v92, v92, v93
	v_cvt_pk_bf16_f32 v93, v186, v187
	s_mov_b64 s[98:99], 0x10000
	v_lshl_add_u64 v[254:255], v[160:161], 0, s[98:99]
	global_store_dwordx4 v[254:255], v[90:93], off
	s_waitcnt vmcnt(25)
; #define PG8_BAR __builtin_amdgcn_s_barrier()
; __device__ __forceinline__ u32x4 pack8(const f32x4 v0, const f32x4 v1) { u32x4 w; w.x = cvt_pk_bf16(v0[0], v0[1]); w.y = cvt_pk_bf16(v0[2], v0[3]); w.z = cvt_pk_bf16(v1[0], v1[1]); w.w = cvt_pk_bf16(v1[2], v1[3]); return w; }
; #define EPI_ROWLOOP for (int ai = 0; ai < 2; ++ai) _Pragma("unroll") for (int m = 0; m < 4; ++m)
;     ...
;         cur = nxt; cB = nB; ++ui;
; #pragma unroll
;         for (int h = 0; h < 2; ++h) { uC[h] = uN[h];
; #pragma unroll
;             for (int i = 0; i < 2; ++i) aoC[h][i] = aoN[h][i]; }
;         if constexpr (ALIGN_EPI) { if (wr == 1) PG8_BAR; }
;     __device__ __forceinline__ void operator()(const f32x4 (&acc)[2][2][4][2], const pg8::Unit& u, int wr, int wc, int fr, int fq) const {
;         const int row0 = u.pm * 256 + wr * 64 + fr, c0 = u.pn * 256 + wc * 32 + 8 * fq;
; #pragma unroll
;         EPI_ROWLOOP { const size_t ro = (size_t)(row0 + ai * 128 + m * 16) * 1024 + c0;
; #pragma unroll
;             for (int bj = 0; bj < 2; ++bj) {
;                 f32x4 r0, r1;
;                 if (resf) { r0 = *(const f32x4*)(resf + ro + bj * 128); r1 = *(const f32x4*)(resf + ro + bj * 128 + 4); }
;                 else { const u32x4 xv = *(const u32x4*)(resb + ro + bj * 128);
;                     r0[0] = __uint_as_float(xv.x << 16); r0[1] = __uint_as_float(xv.x & 0xffff0000u); r0[2] = __uint_as_float(xv.y << 16); r0[3] = __uint_as_float(xv.y & 0xffff0000u);
;                     r1[0] = __uint_as_float(xv.z << 16); r1[1] = __uint_as_float(xv.z & 0xffff0000u); r1[2] = __uint_as_float(xv.w << 16); r1[3] = __uint_as_float(xv.w & 0xffff0000u); }
;                 *(u32x4*)(Y + ro + bj * 128) = pack8(acc[ai][bj][m][0] * sc + r0 * ALPHA, acc[ai][bj][m][1] * sc + r1 * ALPHA);
;             } }
	v_pk_fma_f32 v[88:89], v[196:197], s[12:13], v[88:89] op_sel_hi:[1,0,1]
	v_pk_fma_f32 v[86:87], v[194:195], s[12:13], v[86:87] op_sel_hi:[1,0,1]
	v_pk_fma_f32 v[194:195], v[200:201], s[12:13], v[84:85] op_sel_hi:[1,0,1]
	v_pk_fma_f32 v[84:85], v[198:199], s[12:13], v[82:83] op_sel_hi:[1,0,1]
	v_cvt_pk_bf16_f32 v82, v86, v87
	v_cvt_pk_bf16_f32 v83, v88, v89
	v_cvt_pk_bf16_f32 v84, v84, v85
	v_cvt_pk_bf16_f32 v85, v194, v195
	global_store_dwordx4 v[254:255], v[82:85], off offset:256
	s_waitcnt vmcnt(24)
	v_pk_fma_f32 v[80:81], v[204:205], s[12:13], v[80:81] op_sel_hi:[1,0,1]
	v_pk_fma_f32 v[78:79], v[202:203], s[12:13], v[78:79] op_sel_hi:[1,0,1]
	v_pk_fma_f32 v[202:203], v[208:209], s[12:13], v[76:77] op_sel_hi:[1,0,1]
	v_pk_fma_f32 v[76:77], v[206:207], s[12:13], v[74:75] op_sel_hi:[1,0,1]
	v_cvt_pk_bf16_f32 v74, v78, v79
	v_cvt_pk_bf16_f32 v75, v80, v81
	v_cvt_pk_bf16_f32 v76, v76, v77
	v_cvt_pk_bf16_f32 v77, v202, v203
	s_mov_b64 s[98:99], 0x18000
	v_lshl_add_u64 v[254:255], v[160:161], 0, s[98:99]
	global_store_dwordx4 v[254:255], v[74:77], off
	s_waitcnt vmcnt(23)
	v_pk_fma_f32 v[72:73], v[228:229], s[12:13], v[72:73] op_sel_hi:[1,0,1]
	v_pk_fma_f32 v[70:71], v[226:227], s[12:13], v[70:71] op_sel_hi:[1,0,1]
	v_pk_fma_f32 v[226:227], v[232:233], s[12:13], v[68:69] op_sel_hi:[1,0,1]
	v_pk_fma_f32 v[68:69], v[230:231], s[12:13], v[66:67] op_sel_hi:[1,0,1]
	v_cvt_pk_bf16_f32 v66, v70, v71
	v_cvt_pk_bf16_f32 v67, v72, v73
	v_cvt_pk_bf16_f32 v68, v68, v69
	v_cvt_pk_bf16_f32 v69, v226, v227
	global_store_dwordx4 v[254:255], v[66:69], off offset:256
	s_waitcnt vmcnt(22)
	v_pk_fma_f32 v[64:65], v[236:237], s[12:13], v[64:65] op_sel_hi:[1,0,1]
	v_pk_fma_f32 v[62:63], v[234:235], s[12:13], v[62:63] op_sel_hi:[1,0,1]
	v_pk_fma_f32 v[234:235], v[240:241], s[12:13], v[60:61] op_sel_hi:[1,0,1]
	v_pk_fma_f32 v[60:61], v[238:239], s[12:13], v[58:59] op_sel_hi:[1,0,1]
	v_cvt_pk_bf16_f32 v58, v62, v63
	v_cvt_pk_bf16_f32 v59, v64, v65
	v_cvt_pk_bf16_f32 v60, v60, v61
	v_cvt_pk_bf16_f32 v61, v234, v235
	s_mov_b64 s[98:99], 0x40000
	v_lshl_add_u64 v[254:255], v[160:161], 0, s[98:99]
	global_store_dwordx4 v[254:255], v[58:61], off
	s_waitcnt vmcnt(21)
	v_pk_fma_f32 v[56:57], v[244:245], s[12:13], v[56:57] op_sel_hi:[1,0,1]
	v_pk_fma_f32 v[54:55], v[242:243], s[12:13], v[54:55] op_sel_hi:[1,0,1]
	v_pk_fma_f32 v[242:243], v[248:249], s[12:13], v[52:53] op_sel_hi:[1,0,1]
	v_pk_fma_f32 v[52:53], v[246:247], s[12:13], v[50:51] op_sel_hi:[1,0,1]
	v_cvt_pk_bf16_f32 v50, v54, v55
	v_cvt_pk_bf16_f32 v51, v56, v57
	v_cvt_pk_bf16_f32 v52, v52, v53
	v_cvt_pk_bf16_f32 v53, v242, v243
	global_store_dwordx4 v[254:255], v[50:53], off offset:256
	s_waitcnt vmcnt(20)
	v_pk_fma_f32 v[48:49], v[212:213], s[12:13], v[48:49] op_sel_hi:[1,0,1]
	v_pk_fma_f32 v[46:47], v[210:211], s[12:13], v[46:47] op_sel_hi:[1,0,1]
	v_pk_fma_f32 v[210:211], v[216:217], s[12:13], v[44:45] op_sel_hi:[1,0,1]
	v_pk_fma_f32 v[44:45], v[214:215], s[12:13], v[42:43] op_sel_hi:[1,0,1]
	v_cvt_pk_bf16_f32 v42, v46, v47
	v_cvt_pk_bf16_f32 v43, v48, v49
	v_cvt_pk_bf16_f32 v44, v44, v45
	v_cvt_pk_bf16_f32 v45, v210, v211
	s_mov_b64 s[98:99], 0x48000
	v_lshl_add_u64 v[254:255], v[160:161], 0, s[98:99]
	global_store_dwordx4 v[254:255], v[42:45], off
	s_waitcnt vmcnt(19)
	v_pk_fma_f32 v[40:41], v[220:221], s[12:13], v[40:41] op_sel_hi:[1,0,1]
	v_pk_fma_f32 v[38:39], v[218:219], s[12:13], v[38:39] op_sel_hi:[1,0,1]
	v_pk_fma_f32 v[218:219], v[224:225], s[12:13], v[36:37] op_sel_hi:[1,0,1]
	v_pk_fma_f32 v[36:37], v[222:223], s[12:13], v[34:35] op_sel_hi:[1,0,1]
	v_cvt_pk_bf16_f32 v34, v38, v39
	v_cvt_pk_bf16_f32 v35, v40, v41
	v_cvt_pk_bf16_f32 v36, v36, v37
	v_cvt_pk_bf16_f32 v37, v218, v219
	global_store_dwordx4 v[254:255], v[34:37], off offset:256
	s_waitcnt vmcnt(17)
	v_pk_fma_f32 v[32:33], v[124:125], s[12:13], v[32:33] op_sel_hi:[1,0,1]
	v_pk_fma_f32 v[30:31], v[122:123], s[12:13], v[30:31] op_sel_hi:[1,0,1]
	v_pk_fma_f32 v[122:123], v[128:129], s[12:13], v[28:29] op_sel_hi:[1,0,1]
	v_pk_fma_f32 v[28:29], v[126:127], s[12:13], v[26:27] op_sel_hi:[1,0,1]
	v_cvt_pk_bf16_f32 v26, v30, v31
	v_cvt_pk_bf16_f32 v27, v32, v33
	v_cvt_pk_bf16_f32 v28, v28, v29
	v_cvt_pk_bf16_f32 v29, v122, v123
	s_mov_b64 s[98:99], 0x50000
	v_lshl_add_u64 v[254:255], v[160:161], 0, s[98:99]
	global_store_dwordx4 v[254:255], v[26:29], off
	s_waitcnt vmcnt(15)
	v_pk_fma_f32 v[24:25], v[116:117], s[12:13], v[24:25] op_sel_hi:[1,0,1]
	v_pk_fma_f32 v[22:23], v[114:115], s[12:13], v[22:23] op_sel_hi:[1,0,1]
	v_pk_fma_f32 v[114:115], v[120:121], s[12:13], v[20:21] op_sel_hi:[1,0,1]
	v_pk_fma_f32 v[20:21], v[118:119], s[12:13], v[18:19] op_sel_hi:[1,0,1]
	v_cvt_pk_bf16_f32 v18, v22, v23
	v_cvt_pk_bf16_f32 v19, v24, v25
	v_cvt_pk_bf16_f32 v20, v20, v21
	v_cvt_pk_bf16_f32 v21, v114, v115
	global_store_dwordx4 v[254:255], v[18:21], off offset:256
	s_waitcnt vmcnt(13)
	v_pk_fma_f32 v[16:17], v[108:109], s[12:13], v[16:17] op_sel_hi:[1,0,1]
	v_pk_fma_f32 v[14:15], v[106:107], s[12:13], v[14:15] op_sel_hi:[1,0,1]
	v_pk_fma_f32 v[106:107], v[112:113], s[12:13], v[12:13] op_sel_hi:[1,0,1]
	v_pk_fma_f32 v[12:13], v[110:111], s[12:13], v[10:11] op_sel_hi:[1,0,1]
	v_cvt_pk_bf16_f32 v10, v14, v15
	v_cvt_pk_bf16_f32 v11, v16, v17
	v_cvt_pk_bf16_f32 v12, v12, v13
	v_cvt_pk_bf16_f32 v13, v106, v107
	s_mov_b64 s[98:99], 0x58000
	v_lshl_add_u64 v[254:255], v[160:161], 0, s[98:99]
	global_store_dwordx4 v[254:255], v[10:13], off
	s_waitcnt vmcnt(11)
	v_pk_fma_f32 v[8:9], v[100:101], s[12:13], v[8:9] op_sel_hi:[1,0,1]
	v_pk_fma_f32 v[6:7], v[98:99], s[12:13], v[6:7] op_sel_hi:[1,0,1]
	v_pk_fma_f32 v[98:99], v[104:105], s[12:13], v[4:5] op_sel_hi:[1,0,1]
	v_pk_fma_f32 v[4:5], v[102:103], s[12:13], v[2:3] op_sel_hi:[1,0,1]
	v_cvt_pk_bf16_f32 v2, v6, v7
	v_cvt_pk_bf16_f32 v3, v8, v9
	v_cvt_pk_bf16_f32 v4, v4, v5
	v_cvt_pk_bf16_f32 v5, v98, v99
	global_store_dwordx4 v[254:255], v[2:5], off offset:256
	s_cbranch_vccnz .LBB0_401
	s_andn2_b64 vcc, exec, s[6:7]
	s_cbranch_vccnz .LBB0_400
	s_barrier
	s_branch .LBB0_400

; __device__ __forceinline__ u32x4 pack8(const f32x4 v0, const f32x4 v1) { u32x4 w; w.x = cvt_pk_bf16(v0[0], v0[1]); w.y = cvt_pk_bf16(v0[2], v0[3]); w.z = cvt_pk_bf16(v1[0], v1[1]); w.w = cvt_pk_bf16(v1[2], v1[3]); return w; }
; #define EPI_ROWLOOP for (int ai = 0; ai < 2; ++ai) _Pragma("unroll") for (int m = 0; m < 4; ++m)
;     __device__ __forceinline__ void operator()(const f32x4 (&acc)[2][2][4][2], const pg8::Unit& u, int wr, int wc, int fr, int fq) const {
;         const int row0 = u.pm * 256 + wr * 64 + fr, c0 = u.pn * 256 + wc * 32 + 8 * fq;
; #pragma unroll
;         EPI_ROWLOOP { const size_t ro = (size_t)(row0 + ai * 128 + m * 16) * 1024 + c0;
; #pragma unroll
;             for (int bj = 0; bj < 2; ++bj) {
;                 f32x4 r0, r1;
;                 if (resf) { r0 = *(const f32x4*)(resf + ro + bj * 128); r1 = *(const f32x4*)(resf + ro + bj * 128 + 4); }
;                 else { const u32x4 xv = *(const u32x4*)(resb + ro + bj * 128);
;                     r0[0] = __uint_as_float(xv.x << 16); r0[1] = __uint_as_float(xv.x & 0xffff0000u); r0[2] = __uint_as_float(xv.y << 16); r0[3] = __uint_as_float(xv.y & 0xffff0000u);
;                     r1[0] = __uint_as_float(xv.z << 16); r1[1] = __uint_as_float(xv.z & 0xffff0000u); r1[2] = __uint_as_float(xv.w << 16); r1[3] = __uint_as_float(xv.w & 0xffff0000u); }
;                 *(u32x4*)(Y + ro + bj * 128) = pack8(acc[ai][bj][m][0] * sc + r0 * ALPHA, acc[ai][bj][m][1] * sc + r1 * ALPHA);
;             } }
.LBB0_2363:
	v_lshl_add_u32 v6, s59, 8, v169
	v_lshl_or_b32 v4, s62, 8, v170
	v_ashrrev_i32_e32 v7, 31, v6
	v_ashrrev_i32_e32 v5, 31, v4
	v_lshlrev_b64 v[2:3], 10, v[6:7]
	v_lshl_add_u64 v[2:3], v[2:3], 0, v[4:5]
	v_lshlrev_b64 v[2:3], 1, v[2:3]
	v_lshl_add_u64 v[12:13], s[6:7], 0, v[2:3]
	global_load_dwordx4 v[8:11], v[12:13], off nt
	s_nop 0
	global_load_dwordx4 v[12:15], v[12:13], off offset:256 nt
	s_add_u32 s98, s6, 0x8000
	s_addc_u32 s99, s7, 0
	global_load_dwordx4 v[176:179], v2, s[98:99] nt
	global_load_dwordx4 v[180:183], v2, s[98:99] offset:256 nt
	s_add_u32 s98, s6, 0x10000
	s_addc_u32 s99, s7, 0
	global_load_dwordx4 v[184:187], v2, s[98:99] nt
	global_load_dwordx4 v[188:191], v2, s[98:99] offset:256 nt
	s_add_u32 s98, s6, 0x18000
	s_addc_u32 s99, s7, 0
	global_load_dwordx4 v[192:195], v2, s[98:99] nt
	global_load_dwordx4 v[196:199], v2, s[98:99] offset:256 nt
	s_add_u32 s98, s6, s16
	s_addc_u32 s99, s7, s17
	global_load_dwordx4 v[200:203], v2, s[98:99] nt
	global_load_dwordx4 v[204:207], v2, s[98:99] offset:256 nt
	s_add_u32 s98, s6, s18
	s_addc_u32 s99, s7, s19
	global_load_dwordx4 v[224:227], v2, s[98:99] nt
	global_load_dwordx4 v[228:231], v2, s[98:99] offset:256 nt
	s_add_u32 s98, s6, s20
	s_addc_u32 s99, s7, s21
	global_load_dwordx4 v[232:235], v2, s[98:99] nt
	global_load_dwordx4 v[236:239], v2, s[98:99] offset:256 nt
	s_add_u32 s98, s6, s22
	s_addc_u32 s99, s7, s23
	global_load_dwordx4 v[240:243], v2, s[98:99] nt
	global_load_dwordx4 v[244:247], v2, s[98:99] offset:256 nt
	v_or_b32_e32 v16, 16, v6
	v_ashrrev_i32_e32 v17, 31, v16
	v_lshlrev_b64 v[16:17], 10, v[16:17]
	v_lshl_add_u64 v[16:17], v[16:17], 0, v[4:5]
	v_lshl_add_u64 v[18:19], s[8:9], 0, v[2:3]
	v_lshlrev_b64 v[16:17], 1, v[16:17]
	v_lshl_add_u64 v[20:21], s[6:7], 0, v[16:17]
	v_lshl_add_u64 v[16:17], s[8:9], 0, v[16:17]
	s_andn2_b64 vcc, exec, s[4:5]
	s_mov_b64 s[4:5], -1
	s_waitcnt vmcnt(14)
	v_lshlrev_b32_e32 v22, 16, v8
	v_and_b32_e32 v23, 0xffff0000, v8
	v_lshlrev_b32_e32 v8, 16, v9
	v_and_b32_e32 v9, 0xffff0000, v9
	v_lshlrev_b32_e32 v24, 16, v10
	v_and_b32_e32 v25, 0xffff0000, v10
	v_lshlrev_b32_e32 v10, 16, v11
	v_and_b32_e32 v11, 0xffff0000, v11
	v_lshlrev_b32_e32 v26, 16, v12
	v_and_b32_e32 v27, 0xffff0000, v12
	v_lshlrev_b32_e32 v12, 16, v13
	v_and_b32_e32 v13, 0xffff0000, v13
	v_lshlrev_b32_e32 v28, 16, v14
	v_and_b32_e32 v29, 0xffff0000, v14
	v_lshlrev_b32_e32 v14, 16, v15
	v_and_b32_e32 v15, 0xffff0000, v15
	v_pk_mul_f32 v[22:23], v[22:23], s[12:13] op_sel_hi:[1,0]
	v_pk_mul_f32 v[8:9], v[8:9], s[12:13] op_sel_hi:[1,0]
	v_pk_mul_f32 v[24:25], v[24:25], s[12:13] op_sel_hi:[1,0]
	v_pk_mul_f32 v[10:11], v[10:11], s[12:13] op_sel_hi:[1,0]
	v_pk_mul_f32 v[26:27], v[26:27], s[12:13] op_sel_hi:[1,0]
	v_pk_mul_f32 v[12:13], v[12:13], s[12:13] op_sel_hi:[1,0]
	v_pk_mul_f32 v[28:29], v[28:29], s[12:13] op_sel_hi:[1,0]
	v_pk_mul_f32 v[14:15], v[14:15], s[12:13] op_sel_hi:[1,0]
	v_pk_fma_f32 v[30:31], v[160:161], s[14:15], v[8:9] op_sel_hi:[1,0,1]
	v_pk_fma_f32 v[8:9], v[158:159], s[14:15], v[22:23] op_sel_hi:[1,0,1]
	v_pk_fma_f32 v[22:23], v[156:157], s[14:15], v[10:11] op_sel_hi:[1,0,1]
	v_pk_fma_f32 v[10:11], v[154:155], s[14:15], v[24:25] op_sel_hi:[1,0,1]
	v_pk_fma_f32 v[24:25], v[152:153], s[14:15], v[12:13] op_sel_hi:[1,0,1]
	v_pk_fma_f32 v[12:13], v[150:151], s[14:15], v[26:27] op_sel_hi:[1,0,1]
	v_pk_fma_f32 v[26:27], v[148:149], s[14:15], v[14:15] op_sel_hi:[1,0,1]
	v_pk_fma_f32 v[14:15], v[146:147], s[14:15], v[28:29] op_sel_hi:[1,0,1]
	v_cvt_pk_bf16_f32 v8, v8, v9
	v_cvt_pk_bf16_f32 v9, v30, v31
	v_cvt_pk_bf16_f32 v10, v10, v11
	v_cvt_pk_bf16_f32 v11, v22, v23
	v_cvt_pk_bf16_f32 v12, v12, v13
	v_cvt_pk_bf16_f32 v13, v24, v25
	v_cvt_pk_bf16_f32 v14, v14, v15
	v_cvt_pk_bf16_f32 v15, v26, v27
	global_store_dwordx4 v[18:19], v[8:11], off
	global_store_dwordx4 v[18:19], v[12:15], off offset:256
	s_nop 1
	s_waitcnt vmcnt(14)
	v_mov_b32_e32 v8, v176
	v_mov_b32_e32 v9, v177
	v_mov_b32_e32 v10, v178
	v_mov_b32_e32 v11, v179
	v_mov_b32_e32 v12, v180
	v_mov_b32_e32 v13, v181
	v_mov_b32_e32 v14, v182
	v_mov_b32_e32 v15, v183
	v_or_b32_e32 v18, 32, v6
	v_ashrrev_i32_e32 v19, 31, v18
	v_lshlrev_b64 v[18:19], 10, v[18:19]
	v_lshl_add_u64 v[18:19], v[18:19], 0, v[4:5]
	v_lshlrev_b64 v[18:19], 1, v[18:19]
	v_lshl_add_u64 v[20:21], s[6:7], 0, v[18:19]
	v_or_b32_e32 v6, 48, v6
	v_ashrrev_i32_e32 v7, 31, v6
	v_lshlrev_b64 v[6:7], 10, v[6:7]
	v_lshl_add_u64 v[4:5], v[6:7], 0, v[4:5]
	v_lshl_add_u64 v[18:19], s[8:9], 0, v[18:19]
	v_lshlrev_b32_e32 v22, 16, v8
	v_and_b32_e32 v23, 0xffff0000, v8
	v_lshlrev_b32_e32 v8, 16, v9
	v_and_b32_e32 v9, 0xffff0000, v9
	v_lshlrev_b32_e32 v24, 16, v10
	v_and_b32_e32 v25, 0xffff0000, v10
	v_lshlrev_b32_e32 v10, 16, v11
	v_and_b32_e32 v11, 0xffff0000, v11
	v_lshlrev_b32_e32 v26, 16, v12
	v_and_b32_e32 v27, 0xffff0000, v12
	v_lshlrev_b32_e32 v12, 16, v13
	v_and_b32_e32 v13, 0xffff0000, v13
	v_lshlrev_b32_e32 v28, 16, v14
	v_and_b32_e32 v29, 0xffff0000, v14
	v_lshlrev_b32_e32 v14, 16, v15
	v_and_b32_e32 v15, 0xffff0000, v15
	v_pk_mul_f32 v[22:23], v[22:23], s[12:13] op_sel_hi:[1,0]
	v_pk_mul_f32 v[8:9], v[8:9], s[12:13] op_sel_hi:[1,0]
	v_pk_mul_f32 v[24:25], v[24:25], s[12:13] op_sel_hi:[1,0]
	v_pk_mul_f32 v[10:11], v[10:11], s[12:13] op_sel_hi:[1,0]
	v_pk_mul_f32 v[26:27], v[26:27], s[12:13] op_sel_hi:[1,0]
	v_pk_mul_f32 v[12:13], v[12:13], s[12:13] op_sel_hi:[1,0]
	v_pk_mul_f32 v[28:29], v[28:29], s[12:13] op_sel_hi:[1,0]
	v_pk_mul_f32 v[14:15], v[14:15], s[12:13] op_sel_hi:[1,0]
	v_pk_fma_f32 v[30:31], v[144:145], s[14:15], v[8:9] op_sel_hi:[1,0,1]
	v_pk_fma_f32 v[8:9], v[142:143], s[14:15], v[22:23] op_sel_hi:[1,0,1]
	v_pk_fma_f32 v[22:23], v[140:141], s[14:15], v[10:11] op_sel_hi:[1,0,1]
	v_pk_fma_f32 v[10:11], v[138:139], s[14:15], v[24:25] op_sel_hi:[1,0,1]
	v_pk_fma_f32 v[24:25], v[136:137], s[14:15], v[12:13] op_sel_hi:[1,0,1]
	v_pk_fma_f32 v[12:13], v[134:135], s[14:15], v[26:27] op_sel_hi:[1,0,1]
	v_pk_fma_f32 v[26:27], v[132:133], s[14:15], v[14:15] op_sel_hi:[1,0,1]
	v_pk_fma_f32 v[14:15], v[130:131], s[14:15], v[28:29] op_sel_hi:[1,0,1]
	v_cvt_pk_bf16_f32 v8, v8, v9
	v_cvt_pk_bf16_f32 v9, v30, v31
	v_cvt_pk_bf16_f32 v10, v10, v11
	v_cvt_pk_bf16_f32 v11, v22, v23
	v_cvt_pk_bf16_f32 v12, v12, v13
	v_cvt_pk_bf16_f32 v13, v24, v25
	v_cvt_pk_bf16_f32 v14, v14, v15
	v_cvt_pk_bf16_f32 v15, v26, v27
	global_store_dwordx4 v[16:17], v[8:11], off
	global_store_dwordx4 v[16:17], v[12:15], off offset:256
	s_nop 1
	s_waitcnt vmcnt(14)
; __device__ __forceinline__ u32x4 pack8(const f32x4 v0, const f32x4 v1) { u32x4 w; w.x = cvt_pk_bf16(v0[0], v0[1]); w.y = cvt_pk_bf16(v0[2], v0[3]); w.z = cvt_pk_bf16(v1[0], v1[1]); w.w = cvt_pk_bf16(v1[2], v1[3]); return w; }
; #define EPI_ROWLOOP for (int ai = 0; ai < 2; ++ai) _Pragma("unroll") for (int m = 0; m < 4; ++m)
;     __device__ __forceinline__ void operator()(const f32x4 (&acc)[2][2][4][2], const pg8::Unit& u, int wr, int wc, int fr, int fq) const {
;         const int row0 = u.pm * 256 + wr * 64 + fr, c0 = u.pn * 256 + wc * 32 + 8 * fq;
; #pragma unroll
;         EPI_ROWLOOP { const size_t ro = (size_t)(row0 + ai * 128 + m * 16) * 1024 + c0;
; #pragma unroll
;             for (int bj = 0; bj < 2; ++bj) {
;                 f32x4 r0, r1;
;                 if (resf) { r0 = *(const f32x4*)(resf + ro + bj * 128); r1 = *(const f32x4*)(resf + ro + bj * 128 + 4); }
;                 else { const u32x4 xv = *(const u32x4*)(resb + ro + bj * 128);
;                     r0[0] = __uint_as_float(xv.x << 16); r0[1] = __uint_as_float(xv.x & 0xffff0000u); r0[2] = __uint_as_float(xv.y << 16); r0[3] = __uint_as_float(xv.y & 0xffff0000u);
;                     r1[0] = __uint_as_float(xv.z << 16); r1[1] = __uint_as_float(xv.z & 0xffff0000u); r1[2] = __uint_as_float(xv.w << 16); r1[3] = __uint_as_float(xv.w & 0xffff0000u); }
;                 *(u32x4*)(Y + ro + bj * 128) = pack8(acc[ai][bj][m][0] * sc + r0 * ALPHA, acc[ai][bj][m][1] * sc + r1 * ALPHA);
;             } }
	v_mov_b32_e32 v8, v184
	v_mov_b32_e32 v9, v185
	v_mov_b32_e32 v10, v186
	v_mov_b32_e32 v11, v187
	v_mov_b32_e32 v12, v188
	v_mov_b32_e32 v13, v189
	v_mov_b32_e32 v14, v190
	v_mov_b32_e32 v15, v191
	v_lshlrev_b64 v[16:17], 1, v[4:5]
	v_lshl_add_u64 v[20:21], s[6:7], 0, v[16:17]
	v_lshlrev_b32_e32 v4, 16, v8
	v_and_b32_e32 v5, 0xffff0000, v8
	v_lshlrev_b32_e32 v6, 16, v9
	v_and_b32_e32 v7, 0xffff0000, v9
	v_lshlrev_b32_e32 v8, 16, v10
	v_and_b32_e32 v9, 0xffff0000, v10
	v_lshlrev_b32_e32 v10, 16, v11
	v_and_b32_e32 v11, 0xffff0000, v11
	v_lshlrev_b32_e32 v22, 16, v12
	v_and_b32_e32 v23, 0xffff0000, v12
	v_lshlrev_b32_e32 v12, 16, v13
	v_and_b32_e32 v13, 0xffff0000, v13
	v_lshlrev_b32_e32 v24, 16, v14
	v_and_b32_e32 v25, 0xffff0000, v14
	v_lshlrev_b32_e32 v14, 16, v15
	v_and_b32_e32 v15, 0xffff0000, v15
	v_pk_mul_f32 v[4:5], v[4:5], s[12:13] op_sel_hi:[1,0]
	v_pk_mul_f32 v[6:7], v[6:7], s[12:13] op_sel_hi:[1,0]
	v_pk_mul_f32 v[8:9], v[8:9], s[12:13] op_sel_hi:[1,0]
	v_pk_mul_f32 v[10:11], v[10:11], s[12:13] op_sel_hi:[1,0]
	v_pk_mul_f32 v[22:23], v[22:23], s[12:13] op_sel_hi:[1,0]
	v_pk_mul_f32 v[12:13], v[12:13], s[12:13] op_sel_hi:[1,0]
	v_pk_mul_f32 v[24:25], v[24:25], s[12:13] op_sel_hi:[1,0]
	v_pk_mul_f32 v[14:15], v[14:15], s[12:13] op_sel_hi:[1,0]
	v_pk_fma_f32 v[6:7], v[128:129], s[14:15], v[6:7] op_sel_hi:[1,0,1]
	v_pk_fma_f32 v[4:5], v[126:127], s[14:15], v[4:5] op_sel_hi:[1,0,1]
	v_pk_fma_f32 v[10:11], v[124:125], s[14:15], v[10:11] op_sel_hi:[1,0,1]
	v_pk_fma_f32 v[8:9], v[122:123], s[14:15], v[8:9] op_sel_hi:[1,0,1]
	v_pk_fma_f32 v[12:13], v[120:121], s[14:15], v[12:13] op_sel_hi:[1,0,1]
	v_pk_fma_f32 v[22:23], v[118:119], s[14:15], v[22:23] op_sel_hi:[1,0,1]
	v_pk_fma_f32 v[14:15], v[116:117], s[14:15], v[14:15] op_sel_hi:[1,0,1]
	v_pk_fma_f32 v[24:25], v[114:115], s[14:15], v[24:25] op_sel_hi:[1,0,1]
	v_cvt_pk_bf16_f32 v4, v4, v5
	v_cvt_pk_bf16_f32 v5, v6, v7
	v_cvt_pk_bf16_f32 v6, v8, v9
	v_cvt_pk_bf16_f32 v7, v10, v11
	v_cvt_pk_bf16_f32 v8, v22, v23
	v_cvt_pk_bf16_f32 v9, v12, v13
	v_cvt_pk_bf16_f32 v10, v24, v25
	v_cvt_pk_bf16_f32 v11, v14, v15
	global_store_dwordx4 v[18:19], v[4:7], off
	global_store_dwordx4 v[18:19], v[8:11], off offset:256
	s_nop 1
	s_waitcnt vmcnt(14)
	v_mov_b32_e32 v4, v192
	v_mov_b32_e32 v5, v193
	v_mov_b32_e32 v6, v194
	v_mov_b32_e32 v7, v195
	v_mov_b32_e32 v8, v196
	v_mov_b32_e32 v9, v197
	v_mov_b32_e32 v10, v198
	v_mov_b32_e32 v11, v199
	v_lshl_add_u64 v[12:13], v[2:3], 0, s[16:17]
	v_lshl_add_u64 v[14:15], s[8:9], 0, v[16:17]
	v_lshl_add_u64 v[16:17], s[6:7], 0, v[12:13]
	v_lshl_add_u64 v[12:13], s[8:9], 0, v[12:13]
	v_lshlrev_b32_e32 v18, 16, v4
	v_and_b32_e32 v19, 0xffff0000, v4
	v_lshlrev_b32_e32 v4, 16, v5
	v_and_b32_e32 v5, 0xffff0000, v5
	v_lshlrev_b32_e32 v20, 16, v6
	v_and_b32_e32 v21, 0xffff0000, v6
	v_lshlrev_b32_e32 v6, 16, v7
	v_and_b32_e32 v7, 0xffff0000, v7
	v_lshlrev_b32_e32 v22, 16, v8
	v_and_b32_e32 v23, 0xffff0000, v8
	v_lshlrev_b32_e32 v8, 16, v9
	v_and_b32_e32 v9, 0xffff0000, v9
	v_lshlrev_b32_e32 v24, 16, v10
	v_and_b32_e32 v25, 0xffff0000, v10
	v_lshlrev_b32_e32 v10, 16, v11
	v_and_b32_e32 v11, 0xffff0000, v11
	v_pk_mul_f32 v[18:19], v[18:19], s[12:13] op_sel_hi:[1,0]
	v_pk_mul_f32 v[4:5], v[4:5], s[12:13] op_sel_hi:[1,0]
	v_pk_mul_f32 v[20:21], v[20:21], s[12:13] op_sel_hi:[1,0]
	v_pk_mul_f32 v[6:7], v[6:7], s[12:13] op_sel_hi:[1,0]
	v_pk_mul_f32 v[22:23], v[22:23], s[12:13] op_sel_hi:[1,0]
	v_pk_mul_f32 v[8:9], v[8:9], s[12:13] op_sel_hi:[1,0]
	v_pk_mul_f32 v[24:25], v[24:25], s[12:13] op_sel_hi:[1,0]
	v_pk_mul_f32 v[10:11], v[10:11], s[12:13] op_sel_hi:[1,0]
	v_pk_fma_f32 v[26:27], v[112:113], s[14:15], v[4:5] op_sel_hi:[1,0,1]
	v_pk_fma_f32 v[4:5], v[110:111], s[14:15], v[18:19] op_sel_hi:[1,0,1]
	v_pk_fma_f32 v[18:19], v[108:109], s[14:15], v[6:7] op_sel_hi:[1,0,1]
	v_pk_fma_f32 v[6:7], v[106:107], s[14:15], v[20:21] op_sel_hi:[1,0,1]
	v_pk_fma_f32 v[20:21], v[104:105], s[14:15], v[8:9] op_sel_hi:[1,0,1]
	v_pk_fma_f32 v[8:9], v[102:103], s[14:15], v[22:23] op_sel_hi:[1,0,1]
	v_pk_fma_f32 v[22:23], v[100:101], s[14:15], v[10:11] op_sel_hi:[1,0,1]
	v_pk_fma_f32 v[10:11], v[98:99], s[14:15], v[24:25] op_sel_hi:[1,0,1]
	v_cvt_pk_bf16_f32 v4, v4, v5
	v_cvt_pk_bf16_f32 v5, v26, v27
	v_cvt_pk_bf16_f32 v6, v6, v7
	v_cvt_pk_bf16_f32 v7, v18, v19
	v_cvt_pk_bf16_f32 v8, v8, v9
	v_cvt_pk_bf16_f32 v9, v20, v21
	v_cvt_pk_bf16_f32 v10, v10, v11
	v_cvt_pk_bf16_f32 v11, v22, v23
	global_store_dwordx4 v[14:15], v[4:7], off
	global_store_dwordx4 v[14:15], v[8:11], off offset:256
	s_nop 1
	s_waitcnt vmcnt(14)
; __device__ __forceinline__ u32x4 pack8(const f32x4 v0, const f32x4 v1) { u32x4 w; w.x = cvt_pk_bf16(v0[0], v0[1]); w.y = cvt_pk_bf16(v0[2], v0[3]); w.z = cvt_pk_bf16(v1[0], v1[1]); w.w = cvt_pk_bf16(v1[2], v1[3]); return w; }
; #define EPI_ROWLOOP for (int ai = 0; ai < 2; ++ai) _Pragma("unroll") for (int m = 0; m < 4; ++m)
;     __device__ __forceinline__ void operator()(const f32x4 (&acc)[2][2][4][2], const pg8::Unit& u, int wr, int wc, int fr, int fq) const {
;         const int row0 = u.pm * 256 + wr * 64 + fr, c0 = u.pn * 256 + wc * 32 + 8 * fq;
; #pragma unroll
;         EPI_ROWLOOP { const size_t ro = (size_t)(row0 + ai * 128 + m * 16) * 1024 + c0;
; #pragma unroll
;             for (int bj = 0; bj < 2; ++bj) {
;                 f32x4 r0, r1;
;                 if (resf) { r0 = *(const f32x4*)(resf + ro + bj * 128); r1 = *(const f32x4*)(resf + ro + bj * 128 + 4); }
;                 else { const u32x4 xv = *(const u32x4*)(resb + ro + bj * 128);
;                     r0[0] = __uint_as_float(xv.x << 16); r0[1] = __uint_as_float(xv.x & 0xffff0000u); r0[2] = __uint_as_float(xv.y << 16); r0[3] = __uint_as_float(xv.y & 0xffff0000u);
;                     r1[0] = __uint_as_float(xv.z << 16); r1[1] = __uint_as_float(xv.z & 0xffff0000u); r1[2] = __uint_as_float(xv.w << 16); r1[3] = __uint_as_float(xv.w & 0xffff0000u); }
;                 *(u32x4*)(Y + ro + bj * 128) = pack8(acc[ai][bj][m][0] * sc + r0 * ALPHA, acc[ai][bj][m][1] * sc + r1 * ALPHA);
;             } }
	v_mov_b32_e32 v4, v200
	v_mov_b32_e32 v5, v201
	v_mov_b32_e32 v6, v202
	v_mov_b32_e32 v7, v203
	v_mov_b32_e32 v8, v204
	v_mov_b32_e32 v9, v205
	v_mov_b32_e32 v10, v206
	v_mov_b32_e32 v11, v207
	v_lshl_add_u64 v[14:15], v[2:3], 0, s[18:19]
	v_lshl_add_u64 v[16:17], s[6:7], 0, v[14:15]
	v_lshl_add_u64 v[14:15], s[8:9], 0, v[14:15]
	v_lshlrev_b32_e32 v18, 16, v4
	v_and_b32_e32 v19, 0xffff0000, v4
	v_lshlrev_b32_e32 v4, 16, v5
	v_and_b32_e32 v5, 0xffff0000, v5
	v_lshlrev_b32_e32 v20, 16, v6
	v_and_b32_e32 v21, 0xffff0000, v6
	v_lshlrev_b32_e32 v6, 16, v7
	v_and_b32_e32 v7, 0xffff0000, v7
	v_lshlrev_b32_e32 v22, 16, v8
	v_and_b32_e32 v23, 0xffff0000, v8
	v_lshlrev_b32_e32 v8, 16, v9
	v_and_b32_e32 v9, 0xffff0000, v9
	v_lshlrev_b32_e32 v24, 16, v10
	v_and_b32_e32 v25, 0xffff0000, v10
	v_lshlrev_b32_e32 v10, 16, v11
	v_and_b32_e32 v11, 0xffff0000, v11
	v_pk_mul_f32 v[18:19], v[18:19], s[12:13] op_sel_hi:[1,0]
	v_pk_mul_f32 v[4:5], v[4:5], s[12:13] op_sel_hi:[1,0]
	v_pk_mul_f32 v[20:21], v[20:21], s[12:13] op_sel_hi:[1,0]
	v_pk_mul_f32 v[6:7], v[6:7], s[12:13] op_sel_hi:[1,0]
	v_pk_mul_f32 v[22:23], v[22:23], s[12:13] op_sel_hi:[1,0]
	v_pk_mul_f32 v[8:9], v[8:9], s[12:13] op_sel_hi:[1,0]
	v_pk_mul_f32 v[24:25], v[24:25], s[12:13] op_sel_hi:[1,0]
	v_pk_mul_f32 v[10:11], v[10:11], s[12:13] op_sel_hi:[1,0]
	v_pk_fma_f32 v[26:27], v[96:97], s[14:15], v[4:5] op_sel_hi:[1,0,1]
	v_pk_fma_f32 v[4:5], v[94:95], s[14:15], v[18:19] op_sel_hi:[1,0,1]
	v_pk_fma_f32 v[18:19], v[92:93], s[14:15], v[6:7] op_sel_hi:[1,0,1]
	v_pk_fma_f32 v[6:7], v[90:91], s[14:15], v[20:21] op_sel_hi:[1,0,1]
	v_pk_fma_f32 v[20:21], v[88:89], s[14:15], v[8:9] op_sel_hi:[1,0,1]
	v_pk_fma_f32 v[8:9], v[86:87], s[14:15], v[22:23] op_sel_hi:[1,0,1]
	v_pk_fma_f32 v[22:23], v[84:85], s[14:15], v[10:11] op_sel_hi:[1,0,1]
	v_pk_fma_f32 v[10:11], v[82:83], s[14:15], v[24:25] op_sel_hi:[1,0,1]
	v_cvt_pk_bf16_f32 v4, v4, v5
	v_cvt_pk_bf16_f32 v5, v26, v27
	v_cvt_pk_bf16_f32 v6, v6, v7
	v_cvt_pk_bf16_f32 v7, v18, v19
	v_cvt_pk_bf16_f32 v8, v8, v9
	v_cvt_pk_bf16_f32 v9, v20, v21
	v_cvt_pk_bf16_f32 v10, v10, v11
	v_cvt_pk_bf16_f32 v11, v22, v23
	global_store_dwordx4 v[12:13], v[4:7], off
	global_store_dwordx4 v[12:13], v[8:11], off offset:256
	s_nop 1
	s_waitcnt vmcnt(14)
	v_mov_b32_e32 v4, v224
	v_mov_b32_e32 v5, v225
	v_mov_b32_e32 v6, v226
	v_mov_b32_e32 v7, v227
	v_mov_b32_e32 v8, v228
	v_mov_b32_e32 v9, v229
	v_mov_b32_e32 v10, v230
	v_mov_b32_e32 v11, v231
	v_lshl_add_u64 v[12:13], v[2:3], 0, s[20:21]
	v_lshl_add_u64 v[16:17], s[6:7], 0, v[12:13]
	v_lshl_add_u64 v[12:13], s[8:9], 0, v[12:13]
	v_lshlrev_b32_e32 v18, 16, v4
	v_and_b32_e32 v19, 0xffff0000, v4
	v_lshlrev_b32_e32 v4, 16, v5
	v_and_b32_e32 v5, 0xffff0000, v5
	v_lshlrev_b32_e32 v20, 16, v6
	v_and_b32_e32 v21, 0xffff0000, v6
	v_lshlrev_b32_e32 v6, 16, v7
	v_and_b32_e32 v7, 0xffff0000, v7
	v_lshlrev_b32_e32 v22, 16, v8
	v_and_b32_e32 v23, 0xffff0000, v8
	v_lshlrev_b32_e32 v8, 16, v9
	v_and_b32_e32 v9, 0xffff0000, v9
	v_lshlrev_b32_e32 v24, 16, v10
	v_and_b32_e32 v25, 0xffff0000, v10
	v_lshlrev_b32_e32 v10, 16, v11
	v_and_b32_e32 v11, 0xffff0000, v11
	v_pk_mul_f32 v[18:19], v[18:19], s[12:13] op_sel_hi:[1,0]
	v_pk_mul_f32 v[4:5], v[4:5], s[12:13] op_sel_hi:[1,0]
	v_pk_mul_f32 v[20:21], v[20:21], s[12:13] op_sel_hi:[1,0]
	v_pk_mul_f32 v[6:7], v[6:7], s[12:13] op_sel_hi:[1,0]
	v_pk_mul_f32 v[22:23], v[22:23], s[12:13] op_sel_hi:[1,0]
	v_pk_mul_f32 v[8:9], v[8:9], s[12:13] op_sel_hi:[1,0]
	v_pk_mul_f32 v[24:25], v[24:25], s[12:13] op_sel_hi:[1,0]
	v_pk_mul_f32 v[10:11], v[10:11], s[12:13] op_sel_hi:[1,0]
	v_pk_fma_f32 v[26:27], v[80:81], s[14:15], v[4:5] op_sel_hi:[1,0,1]
	v_pk_fma_f32 v[4:5], v[78:79], s[14:15], v[18:19] op_sel_hi:[1,0,1]
	v_pk_fma_f32 v[18:19], v[76:77], s[14:15], v[6:7] op_sel_hi:[1,0,1]
	v_pk_fma_f32 v[6:7], v[74:75], s[14:15], v[20:21] op_sel_hi:[1,0,1]
	v_pk_fma_f32 v[20:21], v[72:73], s[14:15], v[8:9] op_sel_hi:[1,0,1]
	v_pk_fma_f32 v[8:9], v[70:71], s[14:15], v[22:23] op_sel_hi:[1,0,1]
	v_pk_fma_f32 v[22:23], v[68:69], s[14:15], v[10:11] op_sel_hi:[1,0,1]
	v_pk_fma_f32 v[10:11], v[66:67], s[14:15], v[24:25] op_sel_hi:[1,0,1]
	v_cvt_pk_bf16_f32 v4, v4, v5
	v_cvt_pk_bf16_f32 v5, v26, v27
	v_cvt_pk_bf16_f32 v6, v6, v7
	v_cvt_pk_bf16_f32 v7, v18, v19
	v_cvt_pk_bf16_f32 v8, v8, v9
	v_cvt_pk_bf16_f32 v9, v20, v21
	v_cvt_pk_bf16_f32 v10, v10, v11
	v_cvt_pk_bf16_f32 v11, v22, v23
	global_store_dwordx4 v[14:15], v[4:7], off
	global_store_dwordx4 v[14:15], v[8:11], off offset:256
	s_nop 1
	s_waitcnt vmcnt(14)
; #define PG8_BAR __builtin_amdgcn_s_barrier()
; __device__ __forceinline__ u32x4 pack8(const f32x4 v0, const f32x4 v1) { u32x4 w; w.x = cvt_pk_bf16(v0[0], v0[1]); w.y = cvt_pk_bf16(v0[2], v0[3]); w.z = cvt_pk_bf16(v1[0], v1[1]); w.w = cvt_pk_bf16(v1[2], v1[3]); return w; }
; #define EPI_ROWLOOP for (int ai = 0; ai < 2; ++ai) _Pragma("unroll") for (int m = 0; m < 4; ++m)
;     ...
;         cur = nxt; cB = nB; ++ui;
; #pragma unroll
;         for (int h = 0; h < 2; ++h) { uC[h] = uN[h];
; #pragma unroll
;             for (int i = 0; i < 2; ++i) aoC[h][i] = aoN[h][i]; }
;         if constexpr (ALIGN_EPI) { if (wr == 1) PG8_BAR; }
;     __device__ __forceinline__ void operator()(const f32x4 (&acc)[2][2][4][2], const pg8::Unit& u, int wr, int wc, int fr, int fq) const {
;         const int row0 = u.pm * 256 + wr * 64 + fr, c0 = u.pn * 256 + wc * 32 + 8 * fq;
; #pragma unroll
;         EPI_ROWLOOP { const size_t ro = (size_t)(row0 + ai * 128 + m * 16) * 1024 + c0;
; #pragma unroll
;             for (int bj = 0; bj < 2; ++bj) {
;                 f32x4 r0, r1;
;                 if (resf) { r0 = *(const f32x4*)(resf + ro + bj * 128); r1 = *(const f32x4*)(resf + ro + bj * 128 + 4); }
;                 else { const u32x4 xv = *(const u32x4*)(resb + ro + bj * 128);
;                     r0[0] = __uint_as_float(xv.x << 16); r0[1] = __uint_as_float(xv.x & 0xffff0000u); r0[2] = __uint_as_float(xv.y << 16); r0[3] = __uint_as_float(xv.y & 0xffff0000u);
;                     r1[0] = __uint_as_float(xv.z << 16); r1[1] = __uint_as_float(xv.z & 0xffff0000u); r1[2] = __uint_as_float(xv.w << 16); r1[3] = __uint_as_float(xv.w & 0xffff0000u); }
;                 *(u32x4*)(Y + ro + bj * 128) = pack8(acc[ai][bj][m][0] * sc + r0 * ALPHA, acc[ai][bj][m][1] * sc + r1 * ALPHA);
;             } }
	v_mov_b32_e32 v4, v232
	v_mov_b32_e32 v5, v233
	v_mov_b32_e32 v6, v234
	v_mov_b32_e32 v7, v235
	v_mov_b32_e32 v8, v236
	v_mov_b32_e32 v9, v237
	v_mov_b32_e32 v10, v238
	v_mov_b32_e32 v11, v239
	v_lshl_add_u64 v[14:15], v[2:3], 0, s[22:23]
	v_lshl_add_u64 v[16:17], s[6:7], 0, v[14:15]
	v_lshlrev_b32_e32 v2, 16, v4
	v_and_b32_e32 v3, 0xffff0000, v4
	v_lshlrev_b32_e32 v4, 16, v5
	v_and_b32_e32 v5, 0xffff0000, v5
	v_lshlrev_b32_e32 v18, 16, v6
	v_and_b32_e32 v19, 0xffff0000, v6
	v_lshlrev_b32_e32 v6, 16, v7
	v_and_b32_e32 v7, 0xffff0000, v7
	v_lshlrev_b32_e32 v20, 16, v8
	v_and_b32_e32 v21, 0xffff0000, v8
	v_lshlrev_b32_e32 v8, 16, v9
	v_and_b32_e32 v9, 0xffff0000, v9
	v_lshlrev_b32_e32 v22, 16, v10
	v_and_b32_e32 v23, 0xffff0000, v10
	v_lshlrev_b32_e32 v10, 16, v11
	v_and_b32_e32 v11, 0xffff0000, v11
	v_pk_mul_f32 v[2:3], v[2:3], s[12:13] op_sel_hi:[1,0]
	v_pk_mul_f32 v[4:5], v[4:5], s[12:13] op_sel_hi:[1,0]
	v_pk_mul_f32 v[18:19], v[18:19], s[12:13] op_sel_hi:[1,0]
	v_pk_mul_f32 v[6:7], v[6:7], s[12:13] op_sel_hi:[1,0]
	v_pk_mul_f32 v[20:21], v[20:21], s[12:13] op_sel_hi:[1,0]
	v_pk_mul_f32 v[8:9], v[8:9], s[12:13] op_sel_hi:[1,0]
	v_pk_mul_f32 v[22:23], v[22:23], s[12:13] op_sel_hi:[1,0]
	v_pk_mul_f32 v[10:11], v[10:11], s[12:13] op_sel_hi:[1,0]
	v_pk_fma_f32 v[4:5], v[64:65], s[14:15], v[4:5] op_sel_hi:[1,0,1]
	v_pk_fma_f32 v[2:3], v[62:63], s[14:15], v[2:3] op_sel_hi:[1,0,1]
	v_pk_fma_f32 v[6:7], v[60:61], s[14:15], v[6:7] op_sel_hi:[1,0,1]
	v_pk_fma_f32 v[18:19], v[58:59], s[14:15], v[18:19] op_sel_hi:[1,0,1]
	v_pk_fma_f32 v[8:9], v[52:53], s[14:15], v[8:9] op_sel_hi:[1,0,1]
	v_pk_fma_f32 v[20:21], v[50:51], s[14:15], v[20:21] op_sel_hi:[1,0,1]
	v_pk_fma_f32 v[10:11], v[56:57], s[14:15], v[10:11] op_sel_hi:[1,0,1]
	v_pk_fma_f32 v[22:23], v[54:55], s[14:15], v[22:23] op_sel_hi:[1,0,1]
	v_cvt_pk_bf16_f32 v2, v2, v3
	v_cvt_pk_bf16_f32 v3, v4, v5
	v_cvt_pk_bf16_f32 v4, v18, v19
	v_cvt_pk_bf16_f32 v5, v6, v7
	v_cvt_pk_bf16_f32 v6, v20, v21
	v_cvt_pk_bf16_f32 v7, v8, v9
	v_cvt_pk_bf16_f32 v8, v22, v23
	v_cvt_pk_bf16_f32 v9, v10, v11
	global_store_dwordx4 v[12:13], v[2:5], off
	global_store_dwordx4 v[12:13], v[6:9], off offset:256
	s_nop 1
	s_waitcnt vmcnt(14)
	v_mov_b32_e32 v2, v240
	v_mov_b32_e32 v3, v241
	v_mov_b32_e32 v4, v242
	v_mov_b32_e32 v5, v243
	v_mov_b32_e32 v6, v244
	v_mov_b32_e32 v7, v245
	v_mov_b32_e32 v8, v246
	v_mov_b32_e32 v9, v247
	v_lshl_add_u64 v[10:11], s[8:9], 0, v[14:15]
	v_lshlrev_b32_e32 v12, 16, v2
	v_and_b32_e32 v13, 0xffff0000, v2
	v_lshlrev_b32_e32 v2, 16, v3
	v_and_b32_e32 v3, 0xffff0000, v3
	v_lshlrev_b32_e32 v14, 16, v4
	v_and_b32_e32 v15, 0xffff0000, v4
	v_lshlrev_b32_e32 v4, 16, v5
	v_and_b32_e32 v5, 0xffff0000, v5
	v_lshlrev_b32_e32 v16, 16, v6
	v_and_b32_e32 v17, 0xffff0000, v6
	v_lshlrev_b32_e32 v6, 16, v7
	v_and_b32_e32 v7, 0xffff0000, v7
	v_lshlrev_b32_e32 v18, 16, v8
	v_and_b32_e32 v19, 0xffff0000, v8
	v_lshlrev_b32_e32 v8, 16, v9
	v_and_b32_e32 v9, 0xffff0000, v9
	v_pk_mul_f32 v[12:13], v[12:13], s[12:13] op_sel_hi:[1,0]
	v_pk_mul_f32 v[2:3], v[2:3], s[12:13] op_sel_hi:[1,0]
	v_pk_mul_f32 v[14:15], v[14:15], s[12:13] op_sel_hi:[1,0]
	v_pk_mul_f32 v[4:5], v[4:5], s[12:13] op_sel_hi:[1,0]
	v_pk_mul_f32 v[16:17], v[16:17], s[12:13] op_sel_hi:[1,0]
	v_pk_mul_f32 v[6:7], v[6:7], s[12:13] op_sel_hi:[1,0]
	v_pk_mul_f32 v[18:19], v[18:19], s[12:13] op_sel_hi:[1,0]
	v_pk_mul_f32 v[8:9], v[8:9], s[12:13] op_sel_hi:[1,0]
	v_pk_fma_f32 v[20:21], v[48:49], s[14:15], v[2:3] op_sel_hi:[1,0,1]
	v_pk_fma_f32 v[2:3], v[46:47], s[14:15], v[12:13] op_sel_hi:[1,0,1]
	v_pk_fma_f32 v[12:13], v[44:45], s[14:15], v[4:5] op_sel_hi:[1,0,1]
	v_pk_fma_f32 v[4:5], v[42:43], s[14:15], v[14:15] op_sel_hi:[1,0,1]
	v_pk_fma_f32 v[14:15], v[40:41], s[14:15], v[6:7] op_sel_hi:[1,0,1]
	v_pk_fma_f32 v[6:7], v[38:39], s[14:15], v[16:17] op_sel_hi:[1,0,1]
	v_pk_fma_f32 v[16:17], v[36:37], s[14:15], v[8:9] op_sel_hi:[1,0,1]
	v_pk_fma_f32 v[8:9], v[34:35], s[14:15], v[18:19] op_sel_hi:[1,0,1]
	v_cvt_pk_bf16_f32 v2, v2, v3
	v_cvt_pk_bf16_f32 v3, v20, v21
	v_cvt_pk_bf16_f32 v4, v4, v5
	v_cvt_pk_bf16_f32 v5, v12, v13
	v_cvt_pk_bf16_f32 v6, v6, v7
	v_cvt_pk_bf16_f32 v7, v14, v15
	v_cvt_pk_bf16_f32 v8, v8, v9
	v_cvt_pk_bf16_f32 v9, v16, v17
	global_store_dwordx4 v[10:11], v[2:5], off
	global_store_dwordx4 v[10:11], v[6:9], off offset:256
	s_cbranch_vccnz .LBB0_2352
	s_andn2_b64 vcc, exec, s[2:3]
	s_cbranch_vccnz .LBB0_2351
	s_barrier
	s_branch .LBB0_2351
